# attention row-max chain: p0 half first so the MFMA-to-VALU distance is covered by useful work (no s_nop), canonicalising v_max x,x dropped
# baseline (speedup 1.0000x reference)
.LBB0_1304:
	v_max3_f32 v205, v114, v115, v116
	v_max3_f32 v206, v117, v118, v119
	v_max3_f32 v205, v205, v120, v121
	v_max3_f32 v206, v206, v122, v123
	v_max3_f32 v205, v205, v124, v125
	v_max3_f32 v206, v206, v126, v127
	v_max3_f32 v205, v205, v128, v129
	v_max3_f32 v206, v206, v130, v131
	v_max3_f32 v205, v205, v132, v133
	v_max3_f32 v206, v206, v134, v135
	v_max3_f32 v205, v205, v136, v137
	v_max3_f32 v206, v206, v138, v139
	v_max3_f32 v205, v205, v140, v141
	v_max3_f32 v206, v206, v142, v143
	v_max3_f32 v205, v205, v144, v145
	v_max_f32_e32 v205, v205, v206
	v_mov_b32_e32 v206, v205
	s_nop 1
	v_permlane32_swap_b32_e32 v205, v206
	v_max_f32_e32 v205, v205, v206
	v_cmp_lt_f32_e32 vcc, s69, v205
	s_cbranch_vccz .LBB0_1303
	v_add_f32_e32 v98, 0xc0c00000, v205
	v_max_f32_e32 v205, 0, v98
	v_exp_f32_e64 v206, -v205
	v_add_f32_e32 v201, v201, v205
	v_xor_b32_e32 v98, 0x80000000, v201
	v_mov_b32_e32 v99, v98
	v_mov_b32_e32 v100, v98
	v_mov_b32_e32 v101, v98
	v_mov_b32_e32 v102, v98
	v_mov_b32_e32 v103, v98
	v_mov_b32_e32 v104, v98
	v_mov_b32_e32 v105, v98
	v_mov_b32_e32 v106, v98
	v_mov_b32_e32 v107, v98
	v_mov_b32_e32 v108, v98
	v_mov_b32_e32 v109, v98
	v_mov_b32_e32 v110, v98
	v_mov_b32_e32 v111, v98
	v_mov_b32_e32 v112, v98
	v_mov_b32_e32 v113, v98
	v_cmp_gt_f32_e32 vcc, 1.0, v206
	s_cbranch_vccz .LBB0_1302
	s_and_saveexec_b64 s[0:1], s[2:3]
	s_cbranch_execz .LBB0_1301
	ds_write_b32 v151, v206 offset:49280
	s_branch .LBB0_1301

; #define ISSUE_L(t, so) do { const unsigned so_ = (unsigned)(so); \
;     if ((t) < NT) { const char* kb_ = Kh + KROWB(t); pg8::glds16_s(kb_, koff[0], ldsK + so_); pg8::glds16_s(kb_, koff[1], ldsK + so_ + 1024u); } \
;     if ((t) >= 1) { const char* vb_ = Vh + KROWB((t) - 1); pg8::glds16_s(vb_, voff[0], ldsV + so_); pg8::glds16_s(vb_, voff[1], ldsV + so_ + 1024u); } } while (0)
; #define PBAR() asm volatile("s_waitcnt lgkmcnt(0)\n\ts_barrier" ::: "memory")
; #define PBAR_V0() asm volatile("s_waitcnt vmcnt(0) lgkmcnt(0)\n\ts_barrier" ::: "memory")
; #define YPH() YSOFT(false)
; #define ISSUE_L(t, sl) do { \
;     if ((t) < NT) pg8::glds16_s(Kh + KROWB(t), koff, ldsK + (unsigned)(sl) * 8192u); \
;     if ((t) >= 1 && (t) <= NT) pg8::glds16_s((const char*)V8 + (size_t)((t) - 1) * 8192, voff, ldsV + (unsigned)(sl) * 8192u); } while (0)
; #define PBAR() asm volatile("s_waitcnt lgkmcnt(0)\n\ts_barrier" ::: "memory")
; #define PBAR_V0() asm volatile("s_waitcnt vmcnt(0) lgkmcnt(0)\n\ts_barrier" ::: "memory")
; #define PBAR_V3() asm volatile("s_waitcnt vmcnt(2) lgkmcnt(0)\n\ts_barrier" ::: "memory")
; #define YPH() YSOFT(false)
; __device__ __forceinline__ void attn_unit_f8(const bf16_t* __restrict__ Q, const bf16_t* __restrict__ Kb, const unsigned char* __restrict__ V8, bf16_t* __restrict__ O, ...
;     ...
;       __builtin_amdgcn_s_setprio(1); QKT(sx); PV8(sx); sx = NEXT3(sx);
;       if (t + 2 <= NT) { ISSUE_L(t + 2, si); si = NEXT3(si); }
;       __builtin_amdgcn_s_setprio(0);
;       PBAR();
;       YPH(); if (t + 2 < NT) PBAR_V3(); else PBAR_V0();
.LBB0_1338:
	s_setprio 1
	s_lshl_b32 s0, s26, 13
	v_add_u32_e32 v98, s0, v153
	v_add_u32_e32 v123, v98, v140
	v_add_u32_e32 v122, v98, v139
	ds_read_b128 v[102:105], v123 offset:24576
	ds_read_b128 v[98:101], v122 offset:24576
	v_add_u32_e32 v125, s0, v150
	v_add_u32_e32 v124, s0, v149
	v_mfma_scale_f32_32x32x64_f8f6f4 v[66:81], v[130:137], v[162:169], v[66:81], v187, v187 op_sel_hi:[0,0,0]
	s_add_i32 s0, s28, s64
	s_ashr_i32 s1, s0, 31
	s_lshl_b64 s[0:1], s[0:1], 10
	s_add_u32 s0, s59, s0
	s_addc_u32 s1, s60, s1
	s_lshl_b32 s12, s27, 13
	s_add_i32 s13, s12, s57
	s_waitcnt lgkmcnt(0)
	v_mfma_scale_f32_32x32x64_f8f6f4 v[98:113], v[98:105], v[154:161], v[82:97], v187, v187 op_sel_hi:[0,0,0]
	ds_read_b128 v[118:121], v125
	ds_read_b128 v[114:117], v124
	s_waitcnt lgkmcnt(0)
	v_mfma_scale_f32_32x32x64_f8f6f4 v[2:17], v[130:137], v[114:121], v[2:17], v187, v187 op_sel_hi:[0,0,0]
	ds_read_b128 v[114:117], v124 offset:2048
	ds_read_b128 v[118:121], v125 offset:2048
	s_waitcnt lgkmcnt(0)
	v_mfma_scale_f32_32x32x64_f8f6f4 v[18:33], v[130:137], v[114:121], v[18:33], v187, v187 op_sel_hi:[0,0,0]
	ds_read_b128 v[118:121], v125 offset:4096
	ds_read_b128 v[114:117], v124 offset:4096
	s_waitcnt lgkmcnt(0)
	v_mfma_scale_f32_32x32x64_f8f6f4 v[34:49], v[130:137], v[114:121], v[34:49], v187, v187 op_sel_hi:[0,0,0]
	ds_read_b128 v[114:117], v124 offset:6144
	ds_read_b128 v[118:121], v125 offset:6144
	s_waitcnt lgkmcnt(0)
	v_mfma_scale_f32_32x32x64_f8f6f4 v[50:65], v[130:137], v[114:121], v[50:65], v187, v187 op_sel_hi:[0,0,0]
	ds_read_b128 v[114:117], v122 offset:28672
	ds_read_b128 v[118:121], v123 offset:28672
	s_waitcnt lgkmcnt(0)
	v_mfma_scale_f32_32x32x64_f8f6f4 v[114:129], v[114:121], v[154:161], v[82:97], v187, v187 op_sel_hi:[0,0,0]
	s_mov_b32 m0, s13
	s_nop 0
	global_load_lds_dwordx4 v148, s[0:1]
	s_add_u32 s0, s47, 0x2000
	s_addc_u32 s1, s61, 0
	s_add_i32 s12, s12, s58
	s_mov_b32 m0, s12
	s_nop 0
	global_load_lds_dwordx4 v147, s[0:1]
	s_setprio 0
	v_max3_f32 v142, v98, v99, v100
	v_max3_f32 v143, v101, v102, v103
	v_max3_f32 v142, v142, v104, v105
	v_max3_f32 v143, v143, v106, v107
	v_max3_f32 v142, v142, v108, v109
	v_max3_f32 v143, v143, v110, v111
	v_max3_f32 v142, v142, v112, v113
	v_max3_f32 v143, v143, v114, v115
	v_max3_f32 v142, v142, v116, v117
	v_max3_f32 v143, v143, v118, v119
	v_max3_f32 v142, v142, v120, v121
	v_max3_f32 v143, v143, v122, v123
	v_max3_f32 v142, v142, v124, v125
	v_max3_f32 v143, v143, v126, v127
	v_max3_f32 v142, v142, v128, v129
	v_max_f32_e32 v142, v142, v143
	v_mov_b32_e32 v143, v142
	s_nop 1
	v_permlane32_swap_b32_e32 v142, v143
	s_waitcnt lgkmcnt(0)
	s_barrier
	v_max_f32_e32 v142, v142, v143
	v_cmp_lt_f32_e32 vcc, s69, v142
	s_cbranch_vccz .LBB0_1337
	v_add_f32_e32 v82, 0xc0c00000, v142
	v_max_f32_e32 v142, 0, v82
	v_exp_f32_e64 v143, -v142
	v_add_f32_e32 v138, v138, v142
	v_xor_b32_e32 v82, 0x80000000, v138
	v_mov_b32_e32 v83, v82
	v_mov_b32_e32 v84, v82
	v_mov_b32_e32 v85, v82
	v_mov_b32_e32 v86, v82
	v_mov_b32_e32 v87, v82
	v_mov_b32_e32 v88, v82
	v_mov_b32_e32 v89, v82
	v_mov_b32_e32 v90, v82
	v_mov_b32_e32 v91, v82
	v_mov_b32_e32 v92, v82
	v_mov_b32_e32 v93, v82
	v_mov_b32_e32 v94, v82
	v_mov_b32_e32 v95, v82
	v_mov_b32_e32 v96, v82
	v_mov_b32_e32 v97, v82
	v_cmp_gt_f32_e32 vcc, 1.0, v143
	s_cbranch_vccz .LBB0_1336
	s_and_saveexec_b64 s[0:1], s[2:3]
	s_cbranch_execz .LBB0_1335
	ds_write_b32 v151, v143 offset:49280
	s_branch .LBB0_1335
